# diff softmax: row-max chain only on first tile / when a row sum exceeds 128 (exp to second register set); on top of v034
# baseline (speedup 1.0000x reference)
; __device__ __forceinline__ int crow(int r, int hi) { return (r & 3) + 8 * (r >> 2) + 4 * hi; }
; __device__ __forceinline__ void smax_tile(f32x16& p0, f32x16& p1, float& mhat, float& l_reg, f32x16 (&o)[4], float* al_l, const bool first, int r32, int hi,
;                                           bf16x8& pa0, bf16x8& pa1, bf16x8& pa2, bf16x8& pa3) {
;     ...
;     if (__builtin_expect(first || __any(rm > THRL), 0)) {
;         const float dl = first ? rm : fmaxf(rm, 0.f);
;         mhat += dl;
; #pragma unroll
;         for (int r = 0; r < 16; ++r) { p0[r] -= dl; p1[r] -= dl; }
;         if (!first) { const float f = __builtin_amdgcn_exp2f(-dl); l_reg *= f;
;             if (hi == 0) al_l[r32] = f; asm volatile("s_waitcnt lgkmcnt(0)" ::: "memory");
; #pragma unroll
;             for (int d = 0; d < 4; ++d)
; #pragma unroll
;                 for (int r = 0; r < 16; ++r) o[d][r] *= al_l[crow(r, hi)]; }
;     }
; #pragma unroll
;     for (int r = 0; r < 16; ++r) p0[r] = __builtin_amdgcn_exp2f(p0[r]);
; #pragma unroll
;     for (int r = 0; r < 16; ++r) p1[r] = __builtin_amdgcn_exp2f(p1[r]);
;     float ps = p0[0];
; #pragma unroll
;     for (int r = 1; r < 16; ++r) ps += p0[r];
; #pragma unroll
;     for (int r = 0; r < 16; ++r) ps += p1[r];
;     { auto rr = __builtin_amdgcn_permlane32_swap(__float_as_uint(ps), __float_as_uint(ps), false, false); ps = __uint_as_float(rr[0]) + __uint_as_float(rr[1]); }
;     l_reg += ps;
.LBB0_650:
	v_add_f32_e32 v158, v158, v128
	v_sub_f32_e32 v111, v111, v128
	v_sub_f32_e32 v110, v110, v128
	v_sub_f32_e32 v109, v109, v128
	v_sub_f32_e32 v108, v108, v128
	v_sub_f32_e32 v107, v107, v128
	v_sub_f32_e32 v106, v106, v128
	v_sub_f32_e32 v105, v105, v128
	v_sub_f32_e32 v104, v104, v128
	v_sub_f32_e32 v103, v103, v128
	v_sub_f32_e32 v102, v102, v128
	v_sub_f32_e32 v101, v101, v128
	v_sub_f32_e32 v100, v100, v128
	v_sub_f32_e32 v99, v99, v128
	v_sub_f32_e32 v98, v98, v128
	v_sub_f32_e32 v97, v97, v128
	v_sub_f32_e32 v96, v96, v128
	v_sub_f32_e32 v95, v95, v128
	v_sub_f32_e32 v94, v94, v128
	v_sub_f32_e32 v93, v93, v128
	v_sub_f32_e32 v92, v92, v128
	v_sub_f32_e32 v91, v91, v128
	v_sub_f32_e32 v90, v90, v128
	v_sub_f32_e32 v89, v89, v128
	v_sub_f32_e32 v88, v88, v128
	v_sub_f32_e32 v87, v87, v128
	v_sub_f32_e32 v86, v86, v128
	v_sub_f32_e32 v85, v85, v128
	v_sub_f32_e32 v84, v84, v128
	v_sub_f32_e32 v83, v83, v128
	v_sub_f32_e32 v82, v82, v128
	v_sub_f32_e32 v81, v81, v128
	v_sub_f32_e32 v80, v80, v128
	v_exp_f32_e32 v216, v96
	v_exp_f32_e32 v217, v97
	v_exp_f32_e32 v218, v98
	v_exp_f32_e32 v219, v99
	v_exp_f32_e32 v220, v100
	v_exp_f32_e32 v221, v101
	v_add_f32_e32 v128, v216, v217
	v_exp_f32_e32 v222, v102
	v_add_f32_e32 v128, v218, v128
	v_exp_f32_e32 v223, v103
	v_add_f32_e32 v128, v219, v128
	v_exp_f32_e32 v224, v104
	v_add_f32_e32 v128, v220, v128
	v_exp_f32_e32 v225, v105
	v_add_f32_e32 v128, v221, v128
	v_exp_f32_e32 v226, v106
	v_add_f32_e32 v128, v222, v128
	v_exp_f32_e32 v227, v107
	v_add_f32_e32 v128, v223, v128
	v_exp_f32_e32 v228, v108
	v_add_f32_e32 v128, v224, v128
	v_exp_f32_e32 v229, v109
	v_add_f32_e32 v128, v225, v128
	v_exp_f32_e32 v230, v110
	v_add_f32_e32 v128, v226, v128
	v_exp_f32_e32 v231, v111
	v_add_f32_e32 v128, v227, v128
	v_exp_f32_e32 v200, v80
	v_add_f32_e32 v128, v228, v128
	v_exp_f32_e32 v201, v81
	v_add_f32_e32 v128, v229, v128
	v_exp_f32_e32 v202, v82
	v_add_f32_e32 v128, v230, v128
	v_exp_f32_e32 v203, v83
	v_add_f32_e32 v128, v231, v128
	v_exp_f32_e32 v204, v84
	v_add_f32_e32 v128, v200, v128
	v_exp_f32_e32 v205, v85
	v_add_f32_e32 v128, v201, v128
	v_exp_f32_e32 v206, v86
	v_add_f32_e32 v128, v202, v128
	v_exp_f32_e32 v207, v87
	v_add_f32_e32 v128, v203, v128
	v_exp_f32_e32 v208, v88
	v_add_f32_e32 v128, v204, v128
	v_exp_f32_e32 v209, v89
	v_add_f32_e32 v128, v205, v128
	v_exp_f32_e32 v210, v90
	v_add_f32_e32 v128, v206, v128
	v_exp_f32_e32 v211, v91
	v_add_f32_e32 v128, v207, v128
	v_exp_f32_e32 v212, v92
	v_add_f32_e32 v128, v208, v128
	v_exp_f32_e32 v213, v93
	v_add_f32_e32 v128, v209, v128
	v_exp_f32_e32 v214, v94
	v_add_f32_e32 v128, v210, v128
	v_exp_f32_e32 v215, v95
	v_add_f32_e32 v128, v211, v128
	v_add_f32_e32 v128, v212, v128
	v_add_f32_e32 v128, v213, v128
	v_add_f32_e32 v128, v214, v128
	v_add_f32_e32 v128, v215, v128
	v_mov_b32_e32 v129, v128
	v_cvt_pk_bf16_f32 v162, v216, v217
	v_cvt_pk_bf16_f32 v163, v218, v219
	v_permlane32_swap_b32_e32 v128, v129
	v_add_f32_e32 v128, v128, v129
	s_branch .Lmy_d_tail
.LBB0_651:
	v_exp_f32_e32 v216, v96
	v_exp_f32_e32 v217, v97
	v_exp_f32_e32 v218, v98
	v_exp_f32_e32 v219, v99
	v_exp_f32_e32 v220, v100
	v_exp_f32_e32 v221, v101
	v_add_f32_e32 v128, v216, v217
	v_exp_f32_e32 v222, v102
	v_add_f32_e32 v128, v218, v128
	v_exp_f32_e32 v223, v103
	v_add_f32_e32 v128, v219, v128
	v_exp_f32_e32 v224, v104
	v_add_f32_e32 v128, v220, v128
	v_exp_f32_e32 v225, v105
	v_add_f32_e32 v128, v221, v128
	v_exp_f32_e32 v226, v106
	v_add_f32_e32 v128, v222, v128
	v_exp_f32_e32 v227, v107
	v_add_f32_e32 v128, v223, v128
	v_exp_f32_e32 v228, v108
	v_add_f32_e32 v128, v224, v128
	v_exp_f32_e32 v229, v109
	v_add_f32_e32 v128, v225, v128
	v_exp_f32_e32 v230, v110
	v_add_f32_e32 v128, v226, v128
	v_exp_f32_e32 v231, v111
	v_add_f32_e32 v128, v227, v128
	v_exp_f32_e32 v200, v80
	v_add_f32_e32 v128, v228, v128
	v_exp_f32_e32 v201, v81
	v_add_f32_e32 v128, v229, v128
	v_exp_f32_e32 v202, v82
	v_add_f32_e32 v128, v230, v128
	v_exp_f32_e32 v203, v83
	v_add_f32_e32 v128, v231, v128
	v_exp_f32_e32 v204, v84
	v_add_f32_e32 v128, v200, v128
	v_exp_f32_e32 v205, v85
	v_add_f32_e32 v128, v201, v128
	v_exp_f32_e32 v206, v86
	v_add_f32_e32 v128, v202, v128
	v_exp_f32_e32 v207, v87
	v_add_f32_e32 v128, v203, v128
	v_exp_f32_e32 v208, v88
	v_add_f32_e32 v128, v204, v128
	v_exp_f32_e32 v209, v89
	v_add_f32_e32 v128, v205, v128
	v_exp_f32_e32 v210, v90
	v_add_f32_e32 v128, v206, v128
	v_exp_f32_e32 v211, v91
	v_add_f32_e32 v128, v207, v128
	v_exp_f32_e32 v212, v92
	v_add_f32_e32 v128, v208, v128
	v_exp_f32_e32 v213, v93
	v_add_f32_e32 v128, v209, v128
	v_exp_f32_e32 v214, v94
	v_add_f32_e32 v128, v210, v128
	v_exp_f32_e32 v215, v95
	v_add_f32_e32 v128, v211, v128
	v_add_f32_e32 v128, v212, v128
	v_add_f32_e32 v128, v213, v128
	v_add_f32_e32 v128, v214, v128
	v_add_f32_e32 v128, v215, v128
	v_mov_b32_e32 v129, v128
	v_cvt_pk_bf16_f32 v162, v216, v217
	v_cvt_pk_bf16_f32 v163, v218, v219
	v_permlane32_swap_b32_e32 v128, v129
	v_add_f32_e32 v128, v128, v129
	v_cmp_lt_f32_e32 vcc, 0x43000000, v128
	s_cbranch_vccnz .Lmy_d_slow
; #define SBAR() __builtin_amdgcn_sched_barrier(0)
; __device__ __forceinline__ void smax_tile(f32x16& p0, f32x16& p1, float& mhat, float& l_reg, f32x16 (&o)[4], float* al_l, const bool first, int r32, int hi,
;                                           bf16x8& pa0, bf16x8& pa1, bf16x8& pa2, bf16x8& pa3) {
;     ...
;     l_reg += ps;
;     ...
;     PK4(p0, 0, pa0); PK4(p0, 8, pa1); PK4(p1, 0, pa2); PK4(p1, 8, pa3);
; template <int DQK, bool HASQK, bool HASPV, int J>
; __device__ __forceinline__ void slot_read(bf16x8 (&kf)[DQK / 16][2], s16x4 (&vf)[4][8], const int (&ka_)[4], int vb_) {
;     constexpr int NQS = HASQK ? 2 * (DQK / 16) : 0, NS = NQS + (HASPV ? 16 : 0);
;     if constexpr (J < NQS) { constexpr int d0 = J >> 1, h = J & 1; dsr128<(d0 >> 2) * 128 + h * 32 * DQK * 2>(kf[d0][h], ka_[d0 & 3]); }
;     else if constexpr (J < NS) { constexpr int q = J - NQS, g = q >> 2, d = q & 3; dstr64<v_rd_off(d, g, 0)>(vf[g][2 * d], vb_); dstr64<v_rd_off(d, g, 1)>(vf[g][2 * d + 1], vb_); }
; }
; template <int DQK, bool HASQK, bool HASPV, int J> ...
;     constexpr int NQS = HASQK ? 2 * (DQK / 16) : 0, NS = NQS + (HASPV ? 16 : 0);
;     if constexpr (J < NS) {
;         constexpr int rd1 = (J + 1 < NS) ? ((J + 1 < NQS) ? 1 : 2) : 0, rd2 = (J + 2 < NS) ? ((J + 2 < NQS) ? 1 : 2) : 0, rd3 = (J + 3 < NS) ? ((J + 3 < NQS) ? 1 : 2) : 0, NW = rd1 + rd2 + rd3;
;     ...
;         if constexpr (J < NQS) { constexpr int d0 = J >> 1, h = J & 1;
;             LWN1(kf[d0][h]); SBAR();
;             if constexpr (h == 0) p0 = __builtin_amdgcn_mfma_f32_32x32x16_bf16(kf[d0][0], qr[d0], (d0 == 0) ? negm : p0, 0, 0, 0);
;             else p1 = __builtin_amdgcn_mfma_f32_32x32x16_bf16(kf[d0][1], qr[d0], (d0 == 0) ? negm : p1, 0, 0, 0);
;         } else { constexpr int q = J - NQS, g = q >> 2, d = q & 3;
;             LWN2(vf[g][2 * d], vf[g][2 * d + 1]); SBAR();
;             o[d] = __builtin_amdgcn_mfma_f32_32x32x16_bf16(pa[g], (bf16x8){vf[g][2 * d][0], vf[g][2 * d][1], vf[g][2 * d][2], vf[g][2 * d][3], vf[g][2 * d + 1][0], vf[g][2 * d + 1][1], vf[g][2 * d + 1][2], vf[g][2 * d + 1][3]}, o[d], 0, 0, 0);
;         }
;     ...
;         SBAR();
;         slot_read<DQK, HASQK, HASPV, J + 4>(kf, vf, ka_, vb_);
;         SBAR();
;         slot_run<DQK, HASQK, HASPV, J + 1>(kf, vf, ka_, vb_, qr, p0, p1, negm, o, pa);
;     }
; }
.Lmy_d_tail:
	v_add_f32_e32 v159, v159, v128
	v_cvt_pk_bf16_f32 v164, v220, v221
	v_cvt_pk_bf16_f32 v165, v222, v223
	v_cvt_pk_bf16_f32 v166, v224, v225
	v_cvt_pk_bf16_f32 v167, v226, v227
	v_cvt_pk_bf16_f32 v168, v228, v229
	v_cvt_pk_bf16_f32 v169, v230, v231
	v_cvt_pk_bf16_f32 v132, v200, v201
	v_cvt_pk_bf16_f32 v133, v202, v203
	v_cvt_pk_bf16_f32 v134, v204, v205
	v_cvt_pk_bf16_f32 v135, v206, v207
	v_cvt_pk_bf16_f32 v128, v208, v209
	v_cvt_pk_bf16_f32 v129, v210, v211
	v_cvt_pk_bf16_f32 v130, v212, v213
	v_cvt_pk_bf16_f32 v131, v214, v215
	s_cmp_lg_u32 s86, 0
	s_waitcnt lgkmcnt(0)
	s_barrier
	s_cselect_b32 s46, s87, 0x8000
	s_lshl_b32 s47, s86, 13
	v_add_u32_e32 v81, s47, v141
	v_add_u32_e32 v82, s47, v143
	ds_read_b128 v[170:173], v81 offset:0
	ds_read_b128 v[174:177], v81 offset:0x1000
	ds_read_b128 v[178:181], v82 offset:0
	ds_read_b128 v[182:185], v82 offset:0x1000
	v_xor_b32_e32 v80, 0x80000000, v158
	v_add_u32_e32 v186, s47, v160
	v_add_u32_e32 v187, s47, v161
	v_add_u32_e32 v188, s46, v157
	v_mov_b32_e32 v81, v80
	v_mov_b32_e32 v82, v80
	v_mov_b32_e32 v83, v80
	v_mov_b32_e32 v84, v80
	v_mov_b32_e32 v85, v80
	v_mov_b32_e32 v86, v80
	v_mov_b32_e32 v87, v80
	v_mov_b32_e32 v88, v80
	v_mov_b32_e32 v89, v80
	v_mov_b32_e32 v90, v80
	v_mov_b32_e32 v91, v80
	v_mov_b32_e32 v92, v80
	v_mov_b32_e32 v93, v80
	v_mov_b32_e32 v94, v80
	v_mov_b32_e32 v95, v80
	s_waitcnt lgkmcnt(3)
	s_nop 1
	v_mfma_f32_32x32x16_bf16 v[96:111], v[170:173], v[112:115], v[80:95]
	ds_read_b128 v[170:173], v186 offset:0
	s_waitcnt lgkmcnt(3)
	s_nop 0
	v_mfma_f32_32x32x16_bf16 v[80:95], v[174:177], v[112:115], v[80:95]
	ds_read_b128 v[174:177], v186 offset:0x1000
	s_waitcnt lgkmcnt(3)
	s_nop 0
	v_mfma_f32_32x32x16_bf16 v[96:111], v[178:181], v[116:119], v[96:111]
	ds_read_b128 v[178:181], v187 offset:0
	s_waitcnt lgkmcnt(3)
	s_nop 0
	v_mfma_f32_32x32x16_bf16 v[80:95], v[182:185], v[116:119], v[80:95]
	ds_read_b128 v[182:185], v187 offset:0x1000
	s_waitcnt lgkmcnt(3)
	s_nop 0
	v_mfma_f32_32x32x16_bf16 v[96:111], v[170:173], v[120:123], v[96:111]
	ds_read_b64_tr_b16 v[170:171], v188 offset:0
	ds_read_b64_tr_b16 v[172:173], v188 offset:0x800
	s_waitcnt lgkmcnt(4)
	s_nop 0
	v_mfma_f32_32x32x16_bf16 v[80:95], v[174:177], v[120:123], v[80:95]
	ds_read_b64_tr_b16 v[174:175], v188 offset:0x200
	ds_read_b64_tr_b16 v[176:177], v188 offset:0xa00
	s_waitcnt lgkmcnt(5)
	s_nop 0
	v_mfma_f32_32x32x16_bf16 v[96:111], v[178:181], v[124:127], v[96:111]
	ds_read_b64_tr_b16 v[178:179], v188 offset:0x400
	ds_read_b64_tr_b16 v[180:181], v188 offset:0xc00
	s_waitcnt lgkmcnt(6)
	s_nop 0
	v_mfma_f32_32x32x16_bf16 v[80:95], v[182:185], v[124:127], v[80:95]
	ds_read_b64_tr_b16 v[182:183], v188 offset:0x600
	ds_read_b64_tr_b16 v[184:185], v188 offset:0xe00
	s_waitcnt lgkmcnt(6)
	s_nop 0
	v_mfma_f32_32x32x16_bf16 v[64:79], v[162:165], v[170:173], v[64:79]
	ds_read_b64_tr_b16 v[170:171], v188 offset:0x1000
	ds_read_b64_tr_b16 v[172:173], v188 offset:0x1800
	s_waitcnt lgkmcnt(6)
	s_nop 0
	v_mfma_f32_32x32x16_bf16 v[48:63], v[162:165], v[174:177], v[48:63]
	ds_read_b64_tr_b16 v[174:175], v188 offset:0x1200
	ds_read_b64_tr_b16 v[176:177], v188 offset:0x1a00
	s_waitcnt lgkmcnt(6)
	s_nop 0
	v_mfma_f32_32x32x16_bf16 v[32:47], v[162:165], v[178:181], v[32:47]
	ds_read_b64_tr_b16 v[178:179], v188 offset:0x1400
	ds_read_b64_tr_b16 v[180:181], v188 offset:0x1c00
	s_waitcnt lgkmcnt(6)
	s_nop 0
	v_mfma_f32_32x32x16_bf16 v[16:31], v[162:165], v[182:185], v[16:31]
	ds_read_b64_tr_b16 v[162:163], v188 offset:0x1600
	ds_read_b64_tr_b16 v[164:165], v188 offset:0x1e00
	s_waitcnt lgkmcnt(6)
	s_nop 0
	v_mfma_f32_32x32x16_bf16 v[64:79], v[166:169], v[170:173], v[64:79]
	ds_read_b64_tr_b16 v[170:171], v188 offset:0x2000
	ds_read_b64_tr_b16 v[172:173], v188 offset:0x2800
	s_waitcnt lgkmcnt(6)
	s_nop 0
	v_mfma_f32_32x32x16_bf16 v[48:63], v[166:169], v[174:177], v[48:63]
	ds_read_b64_tr_b16 v[174:175], v188 offset:0x2200
	ds_read_b64_tr_b16 v[176:177], v188 offset:0x2a00
	s_waitcnt lgkmcnt(6)
	s_nop 0
	v_mfma_f32_32x32x16_bf16 v[32:47], v[166:169], v[178:181], v[32:47]
	ds_read_b64_tr_b16 v[178:179], v188 offset:0x2400
	ds_read_b64_tr_b16 v[180:181], v188 offset:0x2c00
	s_waitcnt lgkmcnt(6)
	s_nop 0
	v_mfma_f32_32x32x16_bf16 v[16:31], v[166:169], v[162:165], v[16:31]
	ds_read_b64_tr_b16 v[162:163], v188 offset:0x2600
	ds_read_b64_tr_b16 v[164:165], v188 offset:0x2e00
	s_waitcnt lgkmcnt(6)
	s_nop 0
	v_mfma_f32_32x32x16_bf16 v[64:79], v[132:135], v[170:173], v[64:79]
	ds_read_b64_tr_b16 v[166:167], v188 offset:0x3000
	ds_read_b64_tr_b16 v[168:169], v188 offset:0x3800
	s_waitcnt lgkmcnt(6)
	s_nop 0
	v_mfma_f32_32x32x16_bf16 v[48:63], v[132:135], v[174:177], v[48:63]
	ds_read_b64_tr_b16 v[170:171], v188 offset:0x3200
	ds_read_b64_tr_b16 v[172:173], v188 offset:0x3a00
	s_waitcnt lgkmcnt(6)
	s_nop 0
	v_mfma_f32_32x32x16_bf16 v[32:47], v[132:135], v[178:181], v[32:47]
	ds_read_b64_tr_b16 v[174:175], v188 offset:0x3400
	ds_read_b64_tr_b16 v[176:177], v188 offset:0x3c00
	s_waitcnt lgkmcnt(6)
	s_nop 0
	v_mfma_f32_32x32x16_bf16 v[16:31], v[132:135], v[162:165], v[16:31]
	ds_read_b64_tr_b16 v[132:133], v188 offset:0x3600
	ds_read_b64_tr_b16 v[134:135], v188 offset:0x3e00
	s_waitcnt lgkmcnt(6)
	s_nop 0
	v_mfma_f32_32x32x16_bf16 v[64:79], v[128:131], v[166:169], v[64:79]
	s_waitcnt lgkmcnt(4)
	s_nop 0
	v_mfma_f32_32x32x16_bf16 v[48:63], v[128:131], v[170:173], v[48:63]
	s_waitcnt lgkmcnt(2)
	s_nop 0
	v_mfma_f32_32x32x16_bf16 v[32:47], v[128:131], v[174:177], v[32:47]
	s_waitcnt lgkmcnt(0)
	s_nop 0
	v_mfma_f32_32x32x16_bf16 v[16:31], v[128:131], v[132:135], v[16:31]
	v_lshl_add_u64 v[144:145], v[144:145], 0, s[28:29]
	v_lshl_add_u64 v[146:147], v[146:147], 0, s[28:29]
	v_lshl_add_u64 v[148:149], v[148:149], 0, s[28:29]
	s_waitcnt vmcnt(0)
	s_add_u32 s44, s44, 0x10000
	s_waitcnt lgkmcnt(0)
	s_barrier
	s_addc_u32 s45, s45, 0
	s_cmp_eq_u32 s44, 0x7f0000
	s_cbranch_scc1 .LBB0_662

; __device__ __forceinline__ float vmax3(float x, float y, float z) { float r; asm("v_max3_f32 %0, %1, %2, %3" : "=v"(r) : "v"(x), "v"(y), "v"(z)); return r; }
; __device__ __forceinline__ float vmax2(float x, float y) { float r; asm("v_max_f32 %0, %1, %2" : "=v"(r) : "v"(x), "v"(y)); return r; }
; __device__ __forceinline__ void smax_tile(f32x16& p0, f32x16& p1, float& mhat, float& l_reg, f32x16 (&o)[4], float* al_l, const bool first, int r32, int hi,
;                                           bf16x8& pa0, bf16x8& pa1, bf16x8& pa2, bf16x8& pa3) {
;     float a = vmax3(p0[0], p0[1], p1[0]), b = vmax3(p0[2], p0[3], p1[1]); a = vmax3(a, p1[2], p1[3]);
; #pragma unroll
;     for (int r = 4; r < 16; r += 4) { a = vmax3(a, p0[r], p0[r + 1]); b = vmax3(b, p0[r + 2], p0[r + 3]); a = vmax3(a, p1[r], p1[r + 1]); b = vmax3(b, p1[r + 2], p1[r + 3]); }
;     float rm = vmax2(a, b);
;     { auto rr = __builtin_amdgcn_permlane32_swap(__float_as_uint(rm), __float_as_uint(rm), false, false); rm = vmax2(__uint_as_float(rr[0]), __uint_as_float(rr[1])); }
;     if (__builtin_expect(first || __any(rm > THRL), 0)) {
;         const float dl = first ? rm : fmaxf(rm, 0.f);
.LBB0_654:
	s_add_i32 s46, s86, 1
	s_cmp_lg_u32 s86, 2
	s_cselect_b32 s86, s46, 0
	s_lshl_b32 s87, s86, 14
	s_add_i32 s46, s68, s87
	s_add_i32 m0, s46, 0x6000
	s_addk_i32 s87, 0xc000
	global_load_lds_dwordx4 v[146:147], off
	s_add_i32 m0, s46, 0x6400
	s_cmp_eq_u32 s44, 0
	global_load_lds_dwordx4 v[148:149], off
	s_cbranch_scc0 .LBB0_651
.Lmy_d_slow:
	v_mov_b32_e32 v244, v128
	v_max3_f32 v128, v96, v97, v80
	v_max3_f32 v129, v98, v99, v81
	v_max3_f32 v128, v128, v82, v83
	v_max3_f32 v129, v129, v102, v103
	v_max3_f32 v128, v128, v100, v101
	v_max3_f32 v129, v129, v86, v87
	v_max3_f32 v128, v128, v84, v85
	v_max3_f32 v129, v129, v106, v107
	v_max3_f32 v128, v128, v104, v105
	v_max3_f32 v129, v129, v90, v91
	v_max3_f32 v128, v128, v88, v89
	v_max3_f32 v129, v129, v110, v111
	v_max3_f32 v128, v128, v108, v109
	v_max3_f32 v129, v129, v94, v95
	v_max3_f32 v128, v128, v92, v93
	v_max_f32 v128, v128, v129
	v_mov_b32_e32 v129, v128
	s_nop 0
	s_cmp_eq_u32 s44, 0
	v_permlane32_swap_b32_e32 v128, v129
	v_max_f32 v128, v128, v129
	s_cbranch_scc1 .LBB0_661
	v_cmp_lt_f32_e32 vcc, s79, v128
	s_cbranch_vccz .Lmy_d_noresc
	s_branch .LBB0_660

; __device__ __forceinline__ void smax_tile(f32x16& p0, f32x16& p1, float& mhat, float& l_reg, f32x16 (&o)[4], float* al_l, const bool first, int r32, int hi,
;                                           bf16x8& pa0, bf16x8& pa1, bf16x8& pa2, bf16x8& pa3) {
;     ...
;     if (__builtin_expect(first || __any(rm > THRL), 0)) {
;         const float dl = first ? rm : fmaxf(rm, 0.f);
;         mhat += dl;
; #pragma unroll
;         for (int r = 0; r < 16; ++r) { p0[r] -= dl; p1[r] -= dl; }
;         if (!first) { const float f = __builtin_amdgcn_exp2f(-dl); l_reg *= f;
.Lmy_d_noresc:
	v_mov_b32_e32 v128, v244
	s_branch .Lmy_d_tail
